# v44 + hazard-distance audit: exactly two wait states between v_readlane and its consumer in the MoE ranking loop
# baseline (speedup 1.0000x reference)
; __global__ void __launch_bounds__(NWAVES * 64, 2) mega_fwd(KArgs args) {
;     ...
;                 for (int k = 0; k < 32; ++k) { const int rk = __shfl(rem, k, 32); rank += (rk > rem || (rk == rem && rk > 0 && k < e)) ? 1 : 0; }
.LBB0_1894:
	v_readlane_b32 s7, v37, s4
	v_mov_b32_e32 v5, 1
	s_nop 0
	v_mov_b32_e32 v6, s7
	v_cmp_le_i32_e64 s[22:23], v6, v37
	s_and_saveexec_b64 s[12:13], s[22:23]
	s_cbranch_execz .LBB0_1893
	v_cmp_eq_u32_e64 s[22:23], v6, v37
	v_cmp_lt_i32_e64 s[24:25], 0, v6
	s_and_b64 s[6:7], s[22:23], s[24:25]
	v_cmp_lt_u32_e64 s[22:23], s4, v4
	s_and_b64 s[6:7], s[6:7], s[22:23]
	v_cndmask_b32_e64 v5, 0, 1, s[6:7]
	s_branch .LBB0_1893
